# agg1: next stage's ds_swizzle index broadcasts issued during the current stage's payload (one LDS round trip off every stage chain)
# baseline (speedup 1.0000x reference)
_Z11agg1_kernelPKDF16_PKfS2_PKiS4_S2_S2_PDF16_PfS6_i:
	s_load_dwordx8 s[4:11], s[0:1], 0x0
	s_load_dwordx8 s[12:19], s[0:1], 0x20
	s_load_dwordx4 s[20:23], s[0:1], 0x40
	s_load_dword s24, s[0:1], 0x50
	v_lshlrev_b32_e32 v32, 2, v0
	v_readfirstlane_b32 s25, v0
	s_lshl_b32 s26, s2, 5
	v_and_b32_e32 v64, 7, v0
	v_bfe_u32 v65, v0, 3, 3
	v_and_b32_e32 v45, 31, v0
	s_lshr_b32 s25, s25, 6
	v_lshlrev_b32_e32 v1, 1, v64
	v_add_u32_e32 v46, s26, v45
	s_waitcnt lgkmcnt(0)
	global_load_dword v33, v32, s[14:15]
	global_load_dword v34, v32, s[16:17]
	s_add_i32 s28, s24, -1
	v_cmp_gt_i32_e64 s[38:39], s24, v46
	v_min_i32_e32 v46, s28, v46
	v_lshlrev_b32_e32 v47, 2, v46
	global_load_dword v44, v47, s[10:11]
	global_load_dword v48, v47, s[10:11] offset:4
	s_lshl_b32 s27, s25, 11
	v_lshlrev_b32_e32 v62, 6, v64
	v_add_u32_e32 v62, 0x2000, v62
	v_cmp_eq_u32_e64 s[34:35], 0, v64
	v_lshlrev_b32_e32 v35, 8, v64
	v_lshl_add_u32 v35, v65, 4, v35
	v_add_u32_e32 v63, s27, v35
	v_mov_b32_e32 v36, 0
	v_mov_b32_e32 v37, 0
	v_mov_b32_e32 v38, 0
	v_mov_b32_e32 v39, 0
	s_waitcnt vmcnt(2)
	ds_write2st64_b32 v32, v33, v34 offset0:32 offset1:36
	ds_write_b128 v63, v[36:39]
	ds_write_b128 v63, v[36:39] offset:128
	s_waitcnt vmcnt(0)
	v_sub_u32_e32 v48, v48, v44
	v_add_u32_e32 v48, 1, v48
	v_cndmask_b32_e64 v48, 0, v48, s[38:39]
	v_lshl_or_b32 v40, v48, 5, v45
	s_nop 1
	v_mov_b32_dpp v41, v40 quad_perm:[1,0,3,2] row_mask:0xf bank_mask:0xf
	s_mov_b32 s40, 0x99999999
	s_mov_b32 s41, 0x99999999
	v_min_u32_e32 v42, v40, v41
	v_max_u32_e32 v43, v40, v41
	v_cndmask_b32_e64 v40, v42, v43, s[40:41]
	s_nop 1
	v_mov_b32_dpp v41, v40 quad_perm:[2,3,0,1] row_mask:0xf bank_mask:0xf
	s_mov_b32 s40, 0xc3c3c3c3
	s_mov_b32 s41, 0xc3c3c3c3
	v_min_u32_e32 v42, v40, v41
	v_max_u32_e32 v43, v40, v41
	v_cndmask_b32_e64 v40, v42, v43, s[40:41]
	s_nop 1
	v_mov_b32_dpp v41, v40 quad_perm:[1,0,3,2] row_mask:0xf bank_mask:0xf
	s_mov_b32 s40, 0xa5a5a5a5
	s_mov_b32 s41, 0xa5a5a5a5
	v_min_u32_e32 v42, v40, v41
	v_max_u32_e32 v43, v40, v41
	v_cndmask_b32_e64 v40, v42, v43, s[40:41]
	ds_swizzle_b32 v41, v40 offset:swizzle(SWAP,4)
	s_waitcnt lgkmcnt(0)
	s_mov_b32 s40, 0xf00ff00f
	s_mov_b32 s41, 0xf00ff00f
	v_min_u32_e32 v42, v40, v41
	v_max_u32_e32 v43, v40, v41
	v_cndmask_b32_e64 v40, v42, v43, s[40:41]
	s_nop 1
	v_mov_b32_dpp v41, v40 quad_perm:[2,3,0,1] row_mask:0xf bank_mask:0xf
	s_mov_b32 s40, 0xcc33cc33
	s_mov_b32 s41, 0xcc33cc33
	v_min_u32_e32 v42, v40, v41
	v_max_u32_e32 v43, v40, v41
	v_cndmask_b32_e64 v40, v42, v43, s[40:41]
	s_nop 1
	v_mov_b32_dpp v41, v40 quad_perm:[1,0,3,2] row_mask:0xf bank_mask:0xf
	s_mov_b32 s40, 0xaa55aa55
	s_mov_b32 s41, 0xaa55aa55
	v_min_u32_e32 v42, v40, v41
	v_max_u32_e32 v43, v40, v41
	v_cndmask_b32_e64 v40, v42, v43, s[40:41]
	ds_swizzle_b32 v41, v40 offset:swizzle(SWAP,8)
	s_waitcnt lgkmcnt(0)
	s_mov_b32 s40, 0xff0000ff
	s_mov_b32 s41, 0xff0000ff
	v_min_u32_e32 v42, v40, v41
	v_max_u32_e32 v43, v40, v41
	v_cndmask_b32_e64 v40, v42, v43, s[40:41]
	ds_swizzle_b32 v41, v40 offset:swizzle(SWAP,4)
	s_waitcnt lgkmcnt(0)
	s_mov_b32 s40, 0xf0f00f0f
	s_mov_b32 s41, 0xf0f00f0f
	v_min_u32_e32 v42, v40, v41
	v_max_u32_e32 v43, v40, v41
	v_cndmask_b32_e64 v40, v42, v43, s[40:41]
	s_nop 1
	v_mov_b32_dpp v41, v40 quad_perm:[2,3,0,1] row_mask:0xf bank_mask:0xf
	s_mov_b32 s40, 0xcccc3333
	s_mov_b32 s41, 0xcccc3333
	v_min_u32_e32 v42, v40, v41
	v_max_u32_e32 v43, v40, v41
	v_cndmask_b32_e64 v40, v42, v43, s[40:41]
	s_nop 1
	v_mov_b32_dpp v41, v40 quad_perm:[1,0,3,2] row_mask:0xf bank_mask:0xf
	s_mov_b32 s40, 0xaaaa5555
	s_mov_b32 s41, 0xaaaa5555
	v_min_u32_e32 v42, v40, v41
	v_max_u32_e32 v43, v40, v41
	v_cndmask_b32_e64 v40, v42, v43, s[40:41]
	ds_swizzle_b32 v41, v40 offset:swizzle(SWAP,16)
	s_waitcnt lgkmcnt(0)
	s_mov_b32 s40, 0xffff
	s_mov_b32 s41, 0xffff
	v_min_u32_e32 v42, v40, v41
	v_max_u32_e32 v43, v40, v41
	v_cndmask_b32_e64 v40, v42, v43, s[40:41]
	ds_swizzle_b32 v41, v40 offset:swizzle(SWAP,8)
	s_waitcnt lgkmcnt(0)
	s_mov_b32 s40, 0xff00ff
	s_mov_b32 s41, 0xff00ff
	v_min_u32_e32 v42, v40, v41
	v_max_u32_e32 v43, v40, v41
	v_cndmask_b32_e64 v40, v42, v43, s[40:41]
	ds_swizzle_b32 v41, v40 offset:swizzle(SWAP,4)
	s_waitcnt lgkmcnt(0)
	s_mov_b32 s40, 0xf0f0f0f
	s_mov_b32 s41, 0xf0f0f0f
	v_min_u32_e32 v42, v40, v41
	v_max_u32_e32 v43, v40, v41
	v_cndmask_b32_e64 v40, v42, v43, s[40:41]
	s_nop 1
	v_mov_b32_dpp v41, v40 quad_perm:[2,3,0,1] row_mask:0xf bank_mask:0xf
	s_mov_b32 s40, 0x33333333
	s_mov_b32 s41, 0x33333333
	v_min_u32_e32 v42, v40, v41
	v_max_u32_e32 v43, v40, v41
	v_cndmask_b32_e64 v40, v42, v43, s[40:41]
	s_nop 1
	v_mov_b32_dpp v41, v40 quad_perm:[1,0,3,2] row_mask:0xf bank_mask:0xf
	s_mov_b32 s40, 0x55555555
	s_mov_b32 s41, 0x55555555
	v_min_u32_e32 v42, v40, v41
	v_max_u32_e32 v43, v40, v41
	v_cndmask_b32_e64 v40, v42, v43, s[40:41]
	s_lshl_b32 s40, s25, 3
	v_add_u32_e32 v45, s40, v65
	v_lshlrev_b32_e32 v45, 2, v45
	ds_bpermute_b32 v46, v45, v40
	s_waitcnt lgkmcnt(0)
	v_and_b32_e32 v15, 31, v46
	v_lshrrev_b32_e32 v11, 5, v46
	v_lshlrev_b32_e32 v47, 2, v15
	ds_bpermute_b32 v10, v47, v44
	v_add_u32_e32 v66, s26, v15
	v_min_i32_e32 v66, s28, v66
	v_cmp_lt_u32_e64 s[36:37], 0, v11
	v_lshlrev_b32_e32 v4, 2, v66
	v_lshlrev_b32_e32 v35, 2, v64
	v_lshl_or_b32 v35, v66, 5, v35
	global_load_dword v9, v35, s[8:9]
	v_lshrrev_b32_e32 v3, 3, v15
	v_lshlrev_b32_e32 v3, 11, v3
	v_and_b32_e32 v47, 7, v15
	v_lshl_add_u32 v3, v47, 1, v3
	v_lshl_add_u32 v3, v64, 4, v3
	v_readfirstlane_b32 s29, v11
	s_waitcnt lgkmcnt(0)
	s_barrier
	v_add_u32_e32 v67, v10, v64
	v_lshlrev_b32_e32 v67, 2, v67
	v_mov_b32_e32 v5, s24
	v_mov_b32_e32 v6, s24
	v_mov_b32_e32 v7, s24
	v_mov_b32_e32 v8, s24
	v_mov_b32_e32 v69, s24
	v_cndmask_b32_e64 v5, v5, v66, s[34:35]
	v_cmp_gt_i32_e32 vcc, v11, v64
	s_andn2_b64 s[40:41], vcc, s[34:35]
	s_and_saveexec_b64 s[32:33], s[40:41]
	global_load_dword v5, v67, s[12:13] offset:-4
	s_mov_b64 exec, s[32:33]
	v_add_u32_e32 v68, 8, v64
	v_cmp_gt_i32_e32 vcc, v11, v68
	s_and_saveexec_b64 s[32:33], vcc
	global_load_dword v6, v67, s[12:13] offset:28
	s_mov_b64 exec, s[32:33]
	v_add_u32_e32 v68, 16, v64
	v_cmp_gt_i32_e32 vcc, v11, v68
	s_and_saveexec_b64 s[32:33], vcc
	global_load_dword v7, v67, s[12:13] offset:60
	s_mov_b64 exec, s[32:33]
	v_add_u32_e32 v68, 24, v64
	v_cmp_gt_i32_e32 vcc, v11, v68
	s_and_saveexec_b64 s[32:33], vcc
	global_load_dword v8, v67, s[12:13] offset:92
	s_mov_b64 exec, s[32:33]
	v_add_u32_e32 v68, 32, v64
	v_cmp_gt_i32_e32 vcc, v11, v68
	s_and_saveexec_b64 s[32:33], vcc
	global_load_dword v69, v67, s[12:13] offset:124
	s_mov_b64 exec, s[32:33]
	s_waitcnt vmcnt(0)
	v_lshlrev_b32_e32 v5, 4, v5
	v_lshlrev_b32_e32 v6, 4, v6
	v_lshlrev_b32_e32 v7, 4, v7
	v_lshlrev_b32_e32 v8, 4, v8
	v_lshlrev_b32_e32 v69, 4, v69
	s_mov_b32 s42, 0
	s_mov_b32 s43, 0
	ds_swizzle_b32 v32, v5 offset:swizzle(BITMASK_PERM, "pp000")
	ds_swizzle_b32 v33, v5 offset:swizzle(BITMASK_PERM, "pp001")
	ds_swizzle_b32 v34, v5 offset:swizzle(BITMASK_PERM, "pp010")
	ds_swizzle_b32 v35, v5 offset:swizzle(BITMASK_PERM, "pp011")
	s_cmp_lt_i32 s29, 3
	s_cbranch_scc1 .Lagg_first_half
	s_waitcnt lgkmcnt(0)
	v_or_b32_e32 v32, v32, v1
	v_or_b32_e32 v33, v33, v1
	v_or_b32_e32 v34, v34, v1
	v_or_b32_e32 v35, v35, v1
	global_load_ushort v36, v32, s[6:7]
	global_load_ushort v37, v33, s[6:7]
	global_load_ushort v38, v34, s[6:7]
	global_load_ushort v39, v35, s[6:7]
	v_lshlrev_b32_e32 v32, 3, v32
	v_lshlrev_b32_e32 v33, 3, v33
	v_lshlrev_b32_e32 v34, 3, v34
	v_lshlrev_b32_e32 v35, 3, v35
	global_load_dwordx4 v[40:43], v32, s[4:5]
	global_load_dwordx4 v[44:47], v33, s[4:5]
	global_load_dwordx4 v[48:51], v34, s[4:5]
	global_load_dwordx4 v[52:55], v35, s[4:5]
	ds_swizzle_b32 v32, v5 offset:swizzle(BITMASK_PERM, "pp100")
	ds_swizzle_b32 v33, v5 offset:swizzle(BITMASK_PERM, "pp101")
	ds_swizzle_b32 v34, v5 offset:swizzle(BITMASK_PERM, "pp110")
	ds_swizzle_b32 v35, v5 offset:swizzle(BITMASK_PERM, "pp111")
	s_waitcnt vmcnt(4)
	v_fma_mix_f32 v36, v36, 1.0, v9 op_sel_hi:[1,0,0]
	v_fma_mix_f32 v37, v37, 1.0, v9 op_sel_hi:[1,0,0]
	v_fma_mix_f32 v38, v38, 1.0, v9 op_sel_hi:[1,0,0]
	v_fma_mix_f32 v39, v39, 1.0, v9 op_sel_hi:[1,0,0]
	v_mul_f32_e32 v58, 0x3e4ccccd, v36
	v_mul_f32_e32 v59, 0x3e4ccccd, v37
	v_mul_f32_e32 v60, 0x3e4ccccd, v38
	v_mul_f32_e32 v61, 0x3e4ccccd, v39
	v_max_f32_e32 v36, v36, v58
	v_max_f32_e32 v37, v37, v59
	v_max_f32_e32 v38, v38, v60
	v_max_f32_e32 v39, v39, v61
	v_max3_f32 v56, v36, v37, v38
	v_max_f32_e32 v13, v56, v39
	v_sub_f32_e32 v36, v36, v13
	v_sub_f32_e32 v37, v37, v13
	v_sub_f32_e32 v38, v38, v13
	v_sub_f32_e32 v39, v39, v13
	v_exp_f32_e32 v36, v36
	v_exp_f32_e32 v37, v37
	v_exp_f32_e32 v38, v38
	v_exp_f32_e32 v39, v39
	s_nop 0
	v_add_f32_e32 v14, v36, v37
	v_add_f32_e32 v14, v14, v38
	v_add_f32_e32 v14, v14, v39
	s_waitcnt vmcnt(3)
	v_cvt_scalef32_pk_f16_fp8 v58, v40, 1.0
	v_cvt_scalef32_pk_f16_fp8 v59, v40, 1.0 op_sel:[1,0,0]
	v_cvt_scalef32_pk_f16_fp8 v60, v41, 1.0
	v_cvt_scalef32_pk_f16_fp8 v61, v41, 1.0 op_sel:[1,0,0]
	v_fma_mix_f32 v16, v58, v36, 0 op_sel_hi:[1,0,0]
	v_fma_mix_f32 v17, v58, v36, 0 op_sel:[1,0,0] op_sel_hi:[1,0,0]
	v_fma_mix_f32 v18, v59, v36, 0 op_sel_hi:[1,0,0]
	v_fma_mix_f32 v19, v59, v36, 0 op_sel:[1,0,0] op_sel_hi:[1,0,0]
	v_fma_mix_f32 v20, v60, v36, 0 op_sel_hi:[1,0,0]
	v_fma_mix_f32 v21, v60, v36, 0 op_sel:[1,0,0] op_sel_hi:[1,0,0]
	v_fma_mix_f32 v22, v61, v36, 0 op_sel_hi:[1,0,0]
	v_fma_mix_f32 v23, v61, v36, 0 op_sel:[1,0,0] op_sel_hi:[1,0,0]
	v_cvt_scalef32_pk_f16_fp8 v58, v42, 1.0
	v_cvt_scalef32_pk_f16_fp8 v59, v42, 1.0 op_sel:[1,0,0]
	v_cvt_scalef32_pk_f16_fp8 v60, v43, 1.0
	v_cvt_scalef32_pk_f16_fp8 v61, v43, 1.0 op_sel:[1,0,0]
	v_fma_mix_f32 v24, v58, v36, 0 op_sel_hi:[1,0,0]
	v_fma_mix_f32 v25, v58, v36, 0 op_sel:[1,0,0] op_sel_hi:[1,0,0]
	v_fma_mix_f32 v26, v59, v36, 0 op_sel_hi:[1,0,0]
	v_fma_mix_f32 v27, v59, v36, 0 op_sel:[1,0,0] op_sel_hi:[1,0,0]
	v_fma_mix_f32 v28, v60, v36, 0 op_sel_hi:[1,0,0]
	v_fma_mix_f32 v29, v60, v36, 0 op_sel:[1,0,0] op_sel_hi:[1,0,0]
	v_fma_mix_f32 v30, v61, v36, 0 op_sel_hi:[1,0,0]
	v_fma_mix_f32 v31, v61, v36, 0 op_sel:[1,0,0] op_sel_hi:[1,0,0]
	s_waitcnt vmcnt(2)
	v_cvt_scalef32_pk_f16_fp8 v58, v44, 1.0
	v_cvt_scalef32_pk_f16_fp8 v59, v44, 1.0 op_sel:[1,0,0]
	v_cvt_scalef32_pk_f16_fp8 v60, v45, 1.0
	v_cvt_scalef32_pk_f16_fp8 v61, v45, 1.0 op_sel:[1,0,0]
	v_fma_mix_f32 v16, v58, v37, v16 op_sel_hi:[1,0,0]
	v_fma_mix_f32 v17, v58, v37, v17 op_sel:[1,0,0] op_sel_hi:[1,0,0]
	v_fma_mix_f32 v18, v59, v37, v18 op_sel_hi:[1,0,0]
	v_fma_mix_f32 v19, v59, v37, v19 op_sel:[1,0,0] op_sel_hi:[1,0,0]
	v_fma_mix_f32 v20, v60, v37, v20 op_sel_hi:[1,0,0]
	v_fma_mix_f32 v21, v60, v37, v21 op_sel:[1,0,0] op_sel_hi:[1,0,0]
	v_fma_mix_f32 v22, v61, v37, v22 op_sel_hi:[1,0,0]
	v_fma_mix_f32 v23, v61, v37, v23 op_sel:[1,0,0] op_sel_hi:[1,0,0]
	v_cvt_scalef32_pk_f16_fp8 v58, v46, 1.0
	v_cvt_scalef32_pk_f16_fp8 v59, v46, 1.0 op_sel:[1,0,0]
	v_cvt_scalef32_pk_f16_fp8 v60, v47, 1.0
	v_cvt_scalef32_pk_f16_fp8 v61, v47, 1.0 op_sel:[1,0,0]
	v_fma_mix_f32 v24, v58, v37, v24 op_sel_hi:[1,0,0]
	v_fma_mix_f32 v25, v58, v37, v25 op_sel:[1,0,0] op_sel_hi:[1,0,0]
	v_fma_mix_f32 v26, v59, v37, v26 op_sel_hi:[1,0,0]
	v_fma_mix_f32 v27, v59, v37, v27 op_sel:[1,0,0] op_sel_hi:[1,0,0]
	v_fma_mix_f32 v28, v60, v37, v28 op_sel_hi:[1,0,0]
	v_fma_mix_f32 v29, v60, v37, v29 op_sel:[1,0,0] op_sel_hi:[1,0,0]
	v_fma_mix_f32 v30, v61, v37, v30 op_sel_hi:[1,0,0]
	v_fma_mix_f32 v31, v61, v37, v31 op_sel:[1,0,0] op_sel_hi:[1,0,0]
	s_waitcnt vmcnt(1)
	v_cvt_scalef32_pk_f16_fp8 v58, v48, 1.0
	v_cvt_scalef32_pk_f16_fp8 v59, v48, 1.0 op_sel:[1,0,0]
	v_cvt_scalef32_pk_f16_fp8 v60, v49, 1.0
	v_cvt_scalef32_pk_f16_fp8 v61, v49, 1.0 op_sel:[1,0,0]
	v_fma_mix_f32 v16, v58, v38, v16 op_sel_hi:[1,0,0]
	v_fma_mix_f32 v17, v58, v38, v17 op_sel:[1,0,0] op_sel_hi:[1,0,0]
	v_fma_mix_f32 v18, v59, v38, v18 op_sel_hi:[1,0,0]
	v_fma_mix_f32 v19, v59, v38, v19 op_sel:[1,0,0] op_sel_hi:[1,0,0]
	v_fma_mix_f32 v20, v60, v38, v20 op_sel_hi:[1,0,0]
	v_fma_mix_f32 v21, v60, v38, v21 op_sel:[1,0,0] op_sel_hi:[1,0,0]
	v_fma_mix_f32 v22, v61, v38, v22 op_sel_hi:[1,0,0]
	v_fma_mix_f32 v23, v61, v38, v23 op_sel:[1,0,0] op_sel_hi:[1,0,0]
	v_cvt_scalef32_pk_f16_fp8 v58, v50, 1.0
	v_cvt_scalef32_pk_f16_fp8 v59, v50, 1.0 op_sel:[1,0,0]
	v_cvt_scalef32_pk_f16_fp8 v60, v51, 1.0
	v_cvt_scalef32_pk_f16_fp8 v61, v51, 1.0 op_sel:[1,0,0]
	v_fma_mix_f32 v24, v58, v38, v24 op_sel_hi:[1,0,0]
	v_fma_mix_f32 v25, v58, v38, v25 op_sel:[1,0,0] op_sel_hi:[1,0,0]
	v_fma_mix_f32 v26, v59, v38, v26 op_sel_hi:[1,0,0]
	v_fma_mix_f32 v27, v59, v38, v27 op_sel:[1,0,0] op_sel_hi:[1,0,0]
	v_fma_mix_f32 v28, v60, v38, v28 op_sel_hi:[1,0,0]
	v_fma_mix_f32 v29, v60, v38, v29 op_sel:[1,0,0] op_sel_hi:[1,0,0]
	v_fma_mix_f32 v30, v61, v38, v30 op_sel_hi:[1,0,0]
	v_fma_mix_f32 v31, v61, v38, v31 op_sel:[1,0,0] op_sel_hi:[1,0,0]
	s_waitcnt vmcnt(0)
	v_cvt_scalef32_pk_f16_fp8 v58, v52, 1.0
	v_cvt_scalef32_pk_f16_fp8 v59, v52, 1.0 op_sel:[1,0,0]
	v_cvt_scalef32_pk_f16_fp8 v60, v53, 1.0
	v_cvt_scalef32_pk_f16_fp8 v61, v53, 1.0 op_sel:[1,0,0]
	v_fma_mix_f32 v16, v58, v39, v16 op_sel_hi:[1,0,0]
	v_fma_mix_f32 v17, v58, v39, v17 op_sel:[1,0,0] op_sel_hi:[1,0,0]
	v_fma_mix_f32 v18, v59, v39, v18 op_sel_hi:[1,0,0]
	v_fma_mix_f32 v19, v59, v39, v19 op_sel:[1,0,0] op_sel_hi:[1,0,0]
	v_fma_mix_f32 v20, v60, v39, v20 op_sel_hi:[1,0,0]
	v_fma_mix_f32 v21, v60, v39, v21 op_sel:[1,0,0] op_sel_hi:[1,0,0]
	v_fma_mix_f32 v22, v61, v39, v22 op_sel_hi:[1,0,0]
	v_fma_mix_f32 v23, v61, v39, v23 op_sel:[1,0,0] op_sel_hi:[1,0,0]
	v_cvt_scalef32_pk_f16_fp8 v58, v54, 1.0
	v_cvt_scalef32_pk_f16_fp8 v59, v54, 1.0 op_sel:[1,0,0]
	v_cvt_scalef32_pk_f16_fp8 v60, v55, 1.0
	v_cvt_scalef32_pk_f16_fp8 v61, v55, 1.0 op_sel:[1,0,0]
	v_fma_mix_f32 v24, v58, v39, v24 op_sel_hi:[1,0,0]
	v_fma_mix_f32 v25, v58, v39, v25 op_sel:[1,0,0] op_sel_hi:[1,0,0]
	v_fma_mix_f32 v26, v59, v39, v26 op_sel_hi:[1,0,0]
	v_fma_mix_f32 v27, v59, v39, v27 op_sel:[1,0,0] op_sel_hi:[1,0,0]
	v_fma_mix_f32 v28, v60, v39, v28 op_sel_hi:[1,0,0]
	v_fma_mix_f32 v29, v60, v39, v29 op_sel:[1,0,0] op_sel_hi:[1,0,0]
	v_fma_mix_f32 v30, v61, v39, v30 op_sel_hi:[1,0,0]
	v_fma_mix_f32 v31, v61, v39, v31 op_sel:[1,0,0] op_sel_hi:[1,0,0]
	s_sub_i32 s29, s29, 4
	s_branch .Lagg_B
.Lagg_first_half:
	s_waitcnt lgkmcnt(0)
	v_or_b32_e32 v32, v32, v1
	v_or_b32_e32 v33, v33, v1
	global_load_ushort v36, v32, s[6:7]
	global_load_ushort v37, v33, s[6:7]
	v_lshlrev_b32_e32 v32, 3, v32
	v_lshlrev_b32_e32 v33, 3, v33
	global_load_dwordx4 v[40:43], v32, s[4:5]
	global_load_dwordx4 v[44:47], v33, s[4:5]
	ds_swizzle_b32 v32, v5 offset:swizzle(BITMASK_PERM, "pp100")
	ds_swizzle_b32 v33, v5 offset:swizzle(BITMASK_PERM, "pp101")
	ds_swizzle_b32 v34, v5 offset:swizzle(BITMASK_PERM, "pp110")
	ds_swizzle_b32 v35, v5 offset:swizzle(BITMASK_PERM, "pp111")
	s_waitcnt vmcnt(2)
	v_fma_mix_f32 v36, v36, 1.0, v9 op_sel_hi:[1,0,0]
	v_fma_mix_f32 v37, v37, 1.0, v9 op_sel_hi:[1,0,0]
	v_mul_f32_e32 v58, 0x3e4ccccd, v36
	v_mul_f32_e32 v59, 0x3e4ccccd, v37
	v_max_f32_e32 v36, v36, v58
	v_max_f32_e32 v37, v37, v59
	v_max_f32_e32 v13, v36, v37
	v_sub_f32_e32 v36, v36, v13
	v_sub_f32_e32 v37, v37, v13
	v_exp_f32_e32 v36, v36
	v_exp_f32_e32 v37, v37
	s_nop 0
	v_add_f32_e32 v14, v36, v37
	s_waitcnt vmcnt(1)
	v_cvt_scalef32_pk_f16_fp8 v58, v40, 1.0
	v_cvt_scalef32_pk_f16_fp8 v59, v40, 1.0 op_sel:[1,0,0]
	v_cvt_scalef32_pk_f16_fp8 v60, v41, 1.0
	v_cvt_scalef32_pk_f16_fp8 v61, v41, 1.0 op_sel:[1,0,0]
	v_fma_mix_f32 v16, v58, v36, 0 op_sel_hi:[1,0,0]
	v_fma_mix_f32 v17, v58, v36, 0 op_sel:[1,0,0] op_sel_hi:[1,0,0]
	v_fma_mix_f32 v18, v59, v36, 0 op_sel_hi:[1,0,0]
	v_fma_mix_f32 v19, v59, v36, 0 op_sel:[1,0,0] op_sel_hi:[1,0,0]
	v_fma_mix_f32 v20, v60, v36, 0 op_sel_hi:[1,0,0]
	v_fma_mix_f32 v21, v60, v36, 0 op_sel:[1,0,0] op_sel_hi:[1,0,0]
	v_fma_mix_f32 v22, v61, v36, 0 op_sel_hi:[1,0,0]
	v_fma_mix_f32 v23, v61, v36, 0 op_sel:[1,0,0] op_sel_hi:[1,0,0]
	v_cvt_scalef32_pk_f16_fp8 v58, v42, 1.0
	v_cvt_scalef32_pk_f16_fp8 v59, v42, 1.0 op_sel:[1,0,0]
	v_cvt_scalef32_pk_f16_fp8 v60, v43, 1.0
	v_cvt_scalef32_pk_f16_fp8 v61, v43, 1.0 op_sel:[1,0,0]
	v_fma_mix_f32 v24, v58, v36, 0 op_sel_hi:[1,0,0]
	v_fma_mix_f32 v25, v58, v36, 0 op_sel:[1,0,0] op_sel_hi:[1,0,0]
	v_fma_mix_f32 v26, v59, v36, 0 op_sel_hi:[1,0,0]
	v_fma_mix_f32 v27, v59, v36, 0 op_sel:[1,0,0] op_sel_hi:[1,0,0]
	v_fma_mix_f32 v28, v60, v36, 0 op_sel_hi:[1,0,0]
	v_fma_mix_f32 v29, v60, v36, 0 op_sel:[1,0,0] op_sel_hi:[1,0,0]
	v_fma_mix_f32 v30, v61, v36, 0 op_sel_hi:[1,0,0]
	v_fma_mix_f32 v31, v61, v36, 0 op_sel:[1,0,0] op_sel_hi:[1,0,0]
	s_waitcnt vmcnt(0)
	v_cvt_scalef32_pk_f16_fp8 v58, v44, 1.0
	v_cvt_scalef32_pk_f16_fp8 v59, v44, 1.0 op_sel:[1,0,0]
	v_cvt_scalef32_pk_f16_fp8 v60, v45, 1.0
	v_cvt_scalef32_pk_f16_fp8 v61, v45, 1.0 op_sel:[1,0,0]
	v_fma_mix_f32 v16, v58, v37, v16 op_sel_hi:[1,0,0]
	v_fma_mix_f32 v17, v58, v37, v17 op_sel:[1,0,0] op_sel_hi:[1,0,0]
	v_fma_mix_f32 v18, v59, v37, v18 op_sel_hi:[1,0,0]
	v_fma_mix_f32 v19, v59, v37, v19 op_sel:[1,0,0] op_sel_hi:[1,0,0]
	v_fma_mix_f32 v20, v60, v37, v20 op_sel_hi:[1,0,0]
	v_fma_mix_f32 v21, v60, v37, v21 op_sel:[1,0,0] op_sel_hi:[1,0,0]
	v_fma_mix_f32 v22, v61, v37, v22 op_sel_hi:[1,0,0]
	v_fma_mix_f32 v23, v61, v37, v23 op_sel:[1,0,0] op_sel_hi:[1,0,0]
	v_cvt_scalef32_pk_f16_fp8 v58, v46, 1.0
	v_cvt_scalef32_pk_f16_fp8 v59, v46, 1.0 op_sel:[1,0,0]
	v_cvt_scalef32_pk_f16_fp8 v60, v47, 1.0
	v_cvt_scalef32_pk_f16_fp8 v61, v47, 1.0 op_sel:[1,0,0]
	v_fma_mix_f32 v24, v58, v37, v24 op_sel_hi:[1,0,0]
	v_fma_mix_f32 v25, v58, v37, v25 op_sel:[1,0,0] op_sel_hi:[1,0,0]
	v_fma_mix_f32 v26, v59, v37, v26 op_sel_hi:[1,0,0]
	v_fma_mix_f32 v27, v59, v37, v27 op_sel:[1,0,0] op_sel_hi:[1,0,0]
	v_fma_mix_f32 v28, v60, v37, v28 op_sel_hi:[1,0,0]
	v_fma_mix_f32 v29, v60, v37, v29 op_sel:[1,0,0] op_sel_hi:[1,0,0]
	v_fma_mix_f32 v30, v61, v37, v30 op_sel_hi:[1,0,0]
	v_fma_mix_f32 v31, v61, v37, v31 op_sel:[1,0,0] op_sel_hi:[1,0,0]
	s_branch .Lagg_epi
.Lagg_B:
	s_cmp_lt_i32 s29, 1
	s_cbranch_scc1 .Lagg_epi
	s_cmp_lt_i32 s29, 3
	s_cbranch_scc1 .Lagg_B_half
	s_waitcnt lgkmcnt(0)
	v_or_b32_e32 v32, v32, v1
	v_or_b32_e32 v33, v33, v1
	v_or_b32_e32 v34, v34, v1
	v_or_b32_e32 v35, v35, v1
	global_load_ushort v36, v32, s[6:7]
	global_load_ushort v37, v33, s[6:7]
	global_load_ushort v38, v34, s[6:7]
	global_load_ushort v39, v35, s[6:7]
	v_lshlrev_b32_e32 v32, 3, v32
	v_lshlrev_b32_e32 v33, 3, v33
	v_lshlrev_b32_e32 v34, 3, v34
	v_lshlrev_b32_e32 v35, 3, v35
	global_load_dwordx4 v[40:43], v32, s[4:5]
	global_load_dwordx4 v[44:47], v33, s[4:5]
	global_load_dwordx4 v[48:51], v34, s[4:5]
	global_load_dwordx4 v[52:55], v35, s[4:5]
	ds_swizzle_b32 v32, v6 offset:swizzle(BITMASK_PERM, "pp000")
	ds_swizzle_b32 v33, v6 offset:swizzle(BITMASK_PERM, "pp001")
	ds_swizzle_b32 v34, v6 offset:swizzle(BITMASK_PERM, "pp010")
	ds_swizzle_b32 v35, v6 offset:swizzle(BITMASK_PERM, "pp011")
	s_waitcnt vmcnt(4)
	v_fma_mix_f32 v36, v36, 1.0, v9 op_sel_hi:[1,0,0]
	v_fma_mix_f32 v37, v37, 1.0, v9 op_sel_hi:[1,0,0]
	v_fma_mix_f32 v38, v38, 1.0, v9 op_sel_hi:[1,0,0]
	v_fma_mix_f32 v39, v39, 1.0, v9 op_sel_hi:[1,0,0]
	v_mul_f32_e32 v58, 0x3e4ccccd, v36
	v_mul_f32_e32 v59, 0x3e4ccccd, v37
	v_mul_f32_e32 v60, 0x3e4ccccd, v38
	v_mul_f32_e32 v61, 0x3e4ccccd, v39
	v_max_f32_e32 v36, v36, v58
	v_max_f32_e32 v37, v37, v59
	v_max_f32_e32 v38, v38, v60
	v_max_f32_e32 v39, v39, v61
	v_max3_f32 v56, v13, v36, v37
	v_max3_f32 v12, v56, v38, v39
	v_sub_f32_e32 v57, v13, v12
	v_sub_f32_e32 v36, v36, v12
	v_sub_f32_e32 v37, v37, v12
	v_sub_f32_e32 v38, v38, v12
	v_sub_f32_e32 v39, v39, v12
	v_exp_f32_e32 v57, v57
	v_exp_f32_e32 v36, v36
	v_exp_f32_e32 v37, v37
	v_exp_f32_e32 v38, v38
	v_exp_f32_e32 v39, v39
	v_fma_f32 v14, v14, v57, v36
	v_mul_f32_e32 v16, v16, v57
	v_mul_f32_e32 v17, v17, v57
	v_mul_f32_e32 v18, v18, v57
	v_mul_f32_e32 v19, v19, v57
	v_mul_f32_e32 v20, v20, v57
	v_mul_f32_e32 v21, v21, v57
	v_mul_f32_e32 v22, v22, v57
	v_mul_f32_e32 v23, v23, v57
	v_mul_f32_e32 v24, v24, v57
	v_mul_f32_e32 v25, v25, v57
	v_mul_f32_e32 v26, v26, v57
	v_mul_f32_e32 v27, v27, v57
	v_mul_f32_e32 v28, v28, v57
	v_mul_f32_e32 v29, v29, v57
	v_mul_f32_e32 v30, v30, v57
	v_mul_f32_e32 v31, v31, v57
	v_add_f32_e32 v14, v14, v37
	v_add_f32_e32 v14, v14, v38
	v_add_f32_e32 v14, v14, v39
	s_waitcnt vmcnt(3)
	v_cvt_scalef32_pk_f16_fp8 v58, v40, 1.0
	v_cvt_scalef32_pk_f16_fp8 v59, v40, 1.0 op_sel:[1,0,0]
	v_cvt_scalef32_pk_f16_fp8 v60, v41, 1.0
	v_cvt_scalef32_pk_f16_fp8 v61, v41, 1.0 op_sel:[1,0,0]
	v_fma_mix_f32 v16, v58, v36, v16 op_sel_hi:[1,0,0]
	v_fma_mix_f32 v17, v58, v36, v17 op_sel:[1,0,0] op_sel_hi:[1,0,0]
	v_fma_mix_f32 v18, v59, v36, v18 op_sel_hi:[1,0,0]
	v_fma_mix_f32 v19, v59, v36, v19 op_sel:[1,0,0] op_sel_hi:[1,0,0]
	v_fma_mix_f32 v20, v60, v36, v20 op_sel_hi:[1,0,0]
	v_fma_mix_f32 v21, v60, v36, v21 op_sel:[1,0,0] op_sel_hi:[1,0,0]
	v_fma_mix_f32 v22, v61, v36, v22 op_sel_hi:[1,0,0]
	v_fma_mix_f32 v23, v61, v36, v23 op_sel:[1,0,0] op_sel_hi:[1,0,0]
	v_cvt_scalef32_pk_f16_fp8 v58, v42, 1.0
	v_cvt_scalef32_pk_f16_fp8 v59, v42, 1.0 op_sel:[1,0,0]
	v_cvt_scalef32_pk_f16_fp8 v60, v43, 1.0
	v_cvt_scalef32_pk_f16_fp8 v61, v43, 1.0 op_sel:[1,0,0]
	v_fma_mix_f32 v24, v58, v36, v24 op_sel_hi:[1,0,0]
	v_fma_mix_f32 v25, v58, v36, v25 op_sel:[1,0,0] op_sel_hi:[1,0,0]
	v_fma_mix_f32 v26, v59, v36, v26 op_sel_hi:[1,0,0]
	v_fma_mix_f32 v27, v59, v36, v27 op_sel:[1,0,0] op_sel_hi:[1,0,0]
	v_fma_mix_f32 v28, v60, v36, v28 op_sel_hi:[1,0,0]
	v_fma_mix_f32 v29, v60, v36, v29 op_sel:[1,0,0] op_sel_hi:[1,0,0]
	v_fma_mix_f32 v30, v61, v36, v30 op_sel_hi:[1,0,0]
	v_fma_mix_f32 v31, v61, v36, v31 op_sel:[1,0,0] op_sel_hi:[1,0,0]
	s_waitcnt vmcnt(2)
	v_cvt_scalef32_pk_f16_fp8 v58, v44, 1.0
	v_cvt_scalef32_pk_f16_fp8 v59, v44, 1.0 op_sel:[1,0,0]
	v_cvt_scalef32_pk_f16_fp8 v60, v45, 1.0
	v_cvt_scalef32_pk_f16_fp8 v61, v45, 1.0 op_sel:[1,0,0]
	v_fma_mix_f32 v16, v58, v37, v16 op_sel_hi:[1,0,0]
	v_fma_mix_f32 v17, v58, v37, v17 op_sel:[1,0,0] op_sel_hi:[1,0,0]
	v_fma_mix_f32 v18, v59, v37, v18 op_sel_hi:[1,0,0]
	v_fma_mix_f32 v19, v59, v37, v19 op_sel:[1,0,0] op_sel_hi:[1,0,0]
	v_fma_mix_f32 v20, v60, v37, v20 op_sel_hi:[1,0,0]
	v_fma_mix_f32 v21, v60, v37, v21 op_sel:[1,0,0] op_sel_hi:[1,0,0]
	v_fma_mix_f32 v22, v61, v37, v22 op_sel_hi:[1,0,0]
	v_fma_mix_f32 v23, v61, v37, v23 op_sel:[1,0,0] op_sel_hi:[1,0,0]
	v_cvt_scalef32_pk_f16_fp8 v58, v46, 1.0
	v_cvt_scalef32_pk_f16_fp8 v59, v46, 1.0 op_sel:[1,0,0]
	v_cvt_scalef32_pk_f16_fp8 v60, v47, 1.0
	v_cvt_scalef32_pk_f16_fp8 v61, v47, 1.0 op_sel:[1,0,0]
	v_fma_mix_f32 v24, v58, v37, v24 op_sel_hi:[1,0,0]
	v_fma_mix_f32 v25, v58, v37, v25 op_sel:[1,0,0] op_sel_hi:[1,0,0]
	v_fma_mix_f32 v26, v59, v37, v26 op_sel_hi:[1,0,0]
	v_fma_mix_f32 v27, v59, v37, v27 op_sel:[1,0,0] op_sel_hi:[1,0,0]
	v_fma_mix_f32 v28, v60, v37, v28 op_sel_hi:[1,0,0]
	v_fma_mix_f32 v29, v60, v37, v29 op_sel:[1,0,0] op_sel_hi:[1,0,0]
	v_fma_mix_f32 v30, v61, v37, v30 op_sel_hi:[1,0,0]
	v_fma_mix_f32 v31, v61, v37, v31 op_sel:[1,0,0] op_sel_hi:[1,0,0]
	s_waitcnt vmcnt(1)
	v_cvt_scalef32_pk_f16_fp8 v58, v48, 1.0
	v_cvt_scalef32_pk_f16_fp8 v59, v48, 1.0 op_sel:[1,0,0]
	v_cvt_scalef32_pk_f16_fp8 v60, v49, 1.0
	v_cvt_scalef32_pk_f16_fp8 v61, v49, 1.0 op_sel:[1,0,0]
	v_fma_mix_f32 v16, v58, v38, v16 op_sel_hi:[1,0,0]
	v_fma_mix_f32 v17, v58, v38, v17 op_sel:[1,0,0] op_sel_hi:[1,0,0]
	v_fma_mix_f32 v18, v59, v38, v18 op_sel_hi:[1,0,0]
	v_fma_mix_f32 v19, v59, v38, v19 op_sel:[1,0,0] op_sel_hi:[1,0,0]
	v_fma_mix_f32 v20, v60, v38, v20 op_sel_hi:[1,0,0]
	v_fma_mix_f32 v21, v60, v38, v21 op_sel:[1,0,0] op_sel_hi:[1,0,0]
	v_fma_mix_f32 v22, v61, v38, v22 op_sel_hi:[1,0,0]
	v_fma_mix_f32 v23, v61, v38, v23 op_sel:[1,0,0] op_sel_hi:[1,0,0]
	v_cvt_scalef32_pk_f16_fp8 v58, v50, 1.0
	v_cvt_scalef32_pk_f16_fp8 v59, v50, 1.0 op_sel:[1,0,0]
	v_cvt_scalef32_pk_f16_fp8 v60, v51, 1.0
	v_cvt_scalef32_pk_f16_fp8 v61, v51, 1.0 op_sel:[1,0,0]
	v_fma_mix_f32 v24, v58, v38, v24 op_sel_hi:[1,0,0]
	v_fma_mix_f32 v25, v58, v38, v25 op_sel:[1,0,0] op_sel_hi:[1,0,0]
	v_fma_mix_f32 v26, v59, v38, v26 op_sel_hi:[1,0,0]
	v_fma_mix_f32 v27, v59, v38, v27 op_sel:[1,0,0] op_sel_hi:[1,0,0]
	v_fma_mix_f32 v28, v60, v38, v28 op_sel_hi:[1,0,0]
	v_fma_mix_f32 v29, v60, v38, v29 op_sel:[1,0,0] op_sel_hi:[1,0,0]
	v_fma_mix_f32 v30, v61, v38, v30 op_sel_hi:[1,0,0]
	v_fma_mix_f32 v31, v61, v38, v31 op_sel:[1,0,0] op_sel_hi:[1,0,0]
	s_waitcnt vmcnt(0)
	v_cvt_scalef32_pk_f16_fp8 v58, v52, 1.0
	v_cvt_scalef32_pk_f16_fp8 v59, v52, 1.0 op_sel:[1,0,0]
	v_cvt_scalef32_pk_f16_fp8 v60, v53, 1.0
	v_cvt_scalef32_pk_f16_fp8 v61, v53, 1.0 op_sel:[1,0,0]
	v_fma_mix_f32 v16, v58, v39, v16 op_sel_hi:[1,0,0]
	v_fma_mix_f32 v17, v58, v39, v17 op_sel:[1,0,0] op_sel_hi:[1,0,0]
	v_fma_mix_f32 v18, v59, v39, v18 op_sel_hi:[1,0,0]
	v_fma_mix_f32 v19, v59, v39, v19 op_sel:[1,0,0] op_sel_hi:[1,0,0]
	v_fma_mix_f32 v20, v60, v39, v20 op_sel_hi:[1,0,0]
	v_fma_mix_f32 v21, v60, v39, v21 op_sel:[1,0,0] op_sel_hi:[1,0,0]
	v_fma_mix_f32 v22, v61, v39, v22 op_sel_hi:[1,0,0]
	v_fma_mix_f32 v23, v61, v39, v23 op_sel:[1,0,0] op_sel_hi:[1,0,0]
	v_cvt_scalef32_pk_f16_fp8 v58, v54, 1.0
	v_cvt_scalef32_pk_f16_fp8 v59, v54, 1.0 op_sel:[1,0,0]
	v_cvt_scalef32_pk_f16_fp8 v60, v55, 1.0
	v_cvt_scalef32_pk_f16_fp8 v61, v55, 1.0 op_sel:[1,0,0]
	v_fma_mix_f32 v24, v58, v39, v24 op_sel_hi:[1,0,0]
	v_fma_mix_f32 v25, v58, v39, v25 op_sel:[1,0,0] op_sel_hi:[1,0,0]
	v_fma_mix_f32 v26, v59, v39, v26 op_sel_hi:[1,0,0]
	v_fma_mix_f32 v27, v59, v39, v27 op_sel:[1,0,0] op_sel_hi:[1,0,0]
	v_fma_mix_f32 v28, v60, v39, v28 op_sel_hi:[1,0,0]
	v_fma_mix_f32 v29, v60, v39, v29 op_sel:[1,0,0] op_sel_hi:[1,0,0]
	v_fma_mix_f32 v30, v61, v39, v30 op_sel_hi:[1,0,0]
	v_fma_mix_f32 v31, v61, v39, v31 op_sel:[1,0,0] op_sel_hi:[1,0,0]
	s_sub_i32 s29, s29, 4
	v_mov_b32_e32 v5, v6
	v_mov_b32_e32 v6, v7
	v_mov_b32_e32 v7, v8
	v_mov_b32_e32 v8, v69
	s_add_i32 s43, s43, 1
	s_cmp_lt_i32 s29, 1
	s_cbranch_scc1 .Lagg_epi
	s_cmp_lg_u32 s43, 5
	s_cbranch_scc1 .Lagg_A
	s_add_i32 s42, s42, 40
	s_mov_b32 s43, 0
	v_add_u32_e32 v68, s42, v64
	v_add_u32_e32 v67, v10, v68
	v_lshlrev_b32_e32 v67, 2, v67
	v_mov_b32_e32 v5, s24
	v_mov_b32_e32 v6, s24
	v_mov_b32_e32 v7, s24
	v_mov_b32_e32 v8, s24
	v_mov_b32_e32 v69, s24
	v_cmp_gt_i32_e32 vcc, v11, v68
	s_and_saveexec_b64 s[32:33], vcc
	global_load_dword v5, v67, s[12:13] offset:-4
	s_mov_b64 exec, s[32:33]
	v_add_u32_e32 v68, 8, v68
	v_cmp_gt_i32_e32 vcc, v11, v68
	s_and_saveexec_b64 s[32:33], vcc
	global_load_dword v6, v67, s[12:13] offset:28
	s_mov_b64 exec, s[32:33]
	v_add_u32_e32 v68, 8, v68
	v_cmp_gt_i32_e32 vcc, v11, v68
	s_and_saveexec_b64 s[32:33], vcc
	global_load_dword v7, v67, s[12:13] offset:60
	s_mov_b64 exec, s[32:33]
	v_add_u32_e32 v68, 8, v68
	v_cmp_gt_i32_e32 vcc, v11, v68
	s_and_saveexec_b64 s[32:33], vcc
	global_load_dword v8, v67, s[12:13] offset:92
	s_mov_b64 exec, s[32:33]
	v_add_u32_e32 v68, 8, v68
	v_cmp_gt_i32_e32 vcc, v11, v68
	s_and_saveexec_b64 s[32:33], vcc
	global_load_dword v69, v67, s[12:13] offset:124
	s_mov_b64 exec, s[32:33]
	s_waitcnt vmcnt(0)
	v_lshlrev_b32_e32 v5, 4, v5
	v_lshlrev_b32_e32 v6, 4, v6
	v_lshlrev_b32_e32 v7, 4, v7
	v_lshlrev_b32_e32 v8, 4, v8
	v_lshlrev_b32_e32 v69, 4, v69
	ds_swizzle_b32 v32, v5 offset:swizzle(BITMASK_PERM, "pp000")
	ds_swizzle_b32 v33, v5 offset:swizzle(BITMASK_PERM, "pp001")
	ds_swizzle_b32 v34, v5 offset:swizzle(BITMASK_PERM, "pp010")
	ds_swizzle_b32 v35, v5 offset:swizzle(BITMASK_PERM, "pp011")
.Lagg_A:
	s_cmp_lt_i32 s29, 3
	s_cbranch_scc1 .Lagg_A_half
	s_waitcnt lgkmcnt(0)
	v_or_b32_e32 v32, v32, v1
	v_or_b32_e32 v33, v33, v1
	v_or_b32_e32 v34, v34, v1
	v_or_b32_e32 v35, v35, v1
	global_load_ushort v36, v32, s[6:7]
	global_load_ushort v37, v33, s[6:7]
	global_load_ushort v38, v34, s[6:7]
	global_load_ushort v39, v35, s[6:7]
	v_lshlrev_b32_e32 v32, 3, v32
	v_lshlrev_b32_e32 v33, 3, v33
	v_lshlrev_b32_e32 v34, 3, v34
	v_lshlrev_b32_e32 v35, 3, v35
	global_load_dwordx4 v[40:43], v32, s[4:5]
	global_load_dwordx4 v[44:47], v33, s[4:5]
	global_load_dwordx4 v[48:51], v34, s[4:5]
	global_load_dwordx4 v[52:55], v35, s[4:5]
	ds_swizzle_b32 v32, v5 offset:swizzle(BITMASK_PERM, "pp100")
	ds_swizzle_b32 v33, v5 offset:swizzle(BITMASK_PERM, "pp101")
	ds_swizzle_b32 v34, v5 offset:swizzle(BITMASK_PERM, "pp110")
	ds_swizzle_b32 v35, v5 offset:swizzle(BITMASK_PERM, "pp111")
	s_waitcnt vmcnt(4)
	v_fma_mix_f32 v36, v36, 1.0, v9 op_sel_hi:[1,0,0]
	v_fma_mix_f32 v37, v37, 1.0, v9 op_sel_hi:[1,0,0]
	v_fma_mix_f32 v38, v38, 1.0, v9 op_sel_hi:[1,0,0]
	v_fma_mix_f32 v39, v39, 1.0, v9 op_sel_hi:[1,0,0]
	v_mul_f32_e32 v58, 0x3e4ccccd, v36
	v_mul_f32_e32 v59, 0x3e4ccccd, v37
	v_mul_f32_e32 v60, 0x3e4ccccd, v38
	v_mul_f32_e32 v61, 0x3e4ccccd, v39
	v_max_f32_e32 v36, v36, v58
	v_max_f32_e32 v37, v37, v59
	v_max_f32_e32 v38, v38, v60
	v_max_f32_e32 v39, v39, v61
	v_max3_f32 v56, v12, v36, v37
	v_max3_f32 v13, v56, v38, v39
	v_sub_f32_e32 v57, v12, v13
	v_sub_f32_e32 v36, v36, v13
	v_sub_f32_e32 v37, v37, v13
	v_sub_f32_e32 v38, v38, v13
	v_sub_f32_e32 v39, v39, v13
	v_exp_f32_e32 v57, v57
	v_exp_f32_e32 v36, v36
	v_exp_f32_e32 v37, v37
	v_exp_f32_e32 v38, v38
	v_exp_f32_e32 v39, v39
	v_fma_f32 v14, v14, v57, v36
	v_mul_f32_e32 v16, v16, v57
	v_mul_f32_e32 v17, v17, v57
	v_mul_f32_e32 v18, v18, v57
	v_mul_f32_e32 v19, v19, v57
	v_mul_f32_e32 v20, v20, v57
	v_mul_f32_e32 v21, v21, v57
	v_mul_f32_e32 v22, v22, v57
	v_mul_f32_e32 v23, v23, v57
	v_mul_f32_e32 v24, v24, v57
	v_mul_f32_e32 v25, v25, v57
	v_mul_f32_e32 v26, v26, v57
	v_mul_f32_e32 v27, v27, v57
	v_mul_f32_e32 v28, v28, v57
	v_mul_f32_e32 v29, v29, v57
	v_mul_f32_e32 v30, v30, v57
	v_mul_f32_e32 v31, v31, v57
	v_add_f32_e32 v14, v14, v37
	v_add_f32_e32 v14, v14, v38
	v_add_f32_e32 v14, v14, v39
	s_waitcnt vmcnt(3)
	v_cvt_scalef32_pk_f16_fp8 v58, v40, 1.0
	v_cvt_scalef32_pk_f16_fp8 v59, v40, 1.0 op_sel:[1,0,0]
	v_cvt_scalef32_pk_f16_fp8 v60, v41, 1.0
	v_cvt_scalef32_pk_f16_fp8 v61, v41, 1.0 op_sel:[1,0,0]
	v_fma_mix_f32 v16, v58, v36, v16 op_sel_hi:[1,0,0]
	v_fma_mix_f32 v17, v58, v36, v17 op_sel:[1,0,0] op_sel_hi:[1,0,0]
	v_fma_mix_f32 v18, v59, v36, v18 op_sel_hi:[1,0,0]
	v_fma_mix_f32 v19, v59, v36, v19 op_sel:[1,0,0] op_sel_hi:[1,0,0]
	v_fma_mix_f32 v20, v60, v36, v20 op_sel_hi:[1,0,0]
	v_fma_mix_f32 v21, v60, v36, v21 op_sel:[1,0,0] op_sel_hi:[1,0,0]
	v_fma_mix_f32 v22, v61, v36, v22 op_sel_hi:[1,0,0]
	v_fma_mix_f32 v23, v61, v36, v23 op_sel:[1,0,0] op_sel_hi:[1,0,0]
	v_cvt_scalef32_pk_f16_fp8 v58, v42, 1.0
	v_cvt_scalef32_pk_f16_fp8 v59, v42, 1.0 op_sel:[1,0,0]
	v_cvt_scalef32_pk_f16_fp8 v60, v43, 1.0
	v_cvt_scalef32_pk_f16_fp8 v61, v43, 1.0 op_sel:[1,0,0]
	v_fma_mix_f32 v24, v58, v36, v24 op_sel_hi:[1,0,0]
	v_fma_mix_f32 v25, v58, v36, v25 op_sel:[1,0,0] op_sel_hi:[1,0,0]
	v_fma_mix_f32 v26, v59, v36, v26 op_sel_hi:[1,0,0]
	v_fma_mix_f32 v27, v59, v36, v27 op_sel:[1,0,0] op_sel_hi:[1,0,0]
	v_fma_mix_f32 v28, v60, v36, v28 op_sel_hi:[1,0,0]
	v_fma_mix_f32 v29, v60, v36, v29 op_sel:[1,0,0] op_sel_hi:[1,0,0]
	v_fma_mix_f32 v30, v61, v36, v30 op_sel_hi:[1,0,0]
	v_fma_mix_f32 v31, v61, v36, v31 op_sel:[1,0,0] op_sel_hi:[1,0,0]
	s_waitcnt vmcnt(2)
	v_cvt_scalef32_pk_f16_fp8 v58, v44, 1.0
	v_cvt_scalef32_pk_f16_fp8 v59, v44, 1.0 op_sel:[1,0,0]
	v_cvt_scalef32_pk_f16_fp8 v60, v45, 1.0
	v_cvt_scalef32_pk_f16_fp8 v61, v45, 1.0 op_sel:[1,0,0]
	v_fma_mix_f32 v16, v58, v37, v16 op_sel_hi:[1,0,0]
	v_fma_mix_f32 v17, v58, v37, v17 op_sel:[1,0,0] op_sel_hi:[1,0,0]
	v_fma_mix_f32 v18, v59, v37, v18 op_sel_hi:[1,0,0]
	v_fma_mix_f32 v19, v59, v37, v19 op_sel:[1,0,0] op_sel_hi:[1,0,0]
	v_fma_mix_f32 v20, v60, v37, v20 op_sel_hi:[1,0,0]
	v_fma_mix_f32 v21, v60, v37, v21 op_sel:[1,0,0] op_sel_hi:[1,0,0]
	v_fma_mix_f32 v22, v61, v37, v22 op_sel_hi:[1,0,0]
	v_fma_mix_f32 v23, v61, v37, v23 op_sel:[1,0,0] op_sel_hi:[1,0,0]
	v_cvt_scalef32_pk_f16_fp8 v58, v46, 1.0
	v_cvt_scalef32_pk_f16_fp8 v59, v46, 1.0 op_sel:[1,0,0]
	v_cvt_scalef32_pk_f16_fp8 v60, v47, 1.0
	v_cvt_scalef32_pk_f16_fp8 v61, v47, 1.0 op_sel:[1,0,0]
	v_fma_mix_f32 v24, v58, v37, v24 op_sel_hi:[1,0,0]
	v_fma_mix_f32 v25, v58, v37, v25 op_sel:[1,0,0] op_sel_hi:[1,0,0]
	v_fma_mix_f32 v26, v59, v37, v26 op_sel_hi:[1,0,0]
	v_fma_mix_f32 v27, v59, v37, v27 op_sel:[1,0,0] op_sel_hi:[1,0,0]
	v_fma_mix_f32 v28, v60, v37, v28 op_sel_hi:[1,0,0]
	v_fma_mix_f32 v29, v60, v37, v29 op_sel:[1,0,0] op_sel_hi:[1,0,0]
	v_fma_mix_f32 v30, v61, v37, v30 op_sel_hi:[1,0,0]
	v_fma_mix_f32 v31, v61, v37, v31 op_sel:[1,0,0] op_sel_hi:[1,0,0]
	s_waitcnt vmcnt(1)
	v_cvt_scalef32_pk_f16_fp8 v58, v48, 1.0
	v_cvt_scalef32_pk_f16_fp8 v59, v48, 1.0 op_sel:[1,0,0]
	v_cvt_scalef32_pk_f16_fp8 v60, v49, 1.0
	v_cvt_scalef32_pk_f16_fp8 v61, v49, 1.0 op_sel:[1,0,0]
	v_fma_mix_f32 v16, v58, v38, v16 op_sel_hi:[1,0,0]
	v_fma_mix_f32 v17, v58, v38, v17 op_sel:[1,0,0] op_sel_hi:[1,0,0]
	v_fma_mix_f32 v18, v59, v38, v18 op_sel_hi:[1,0,0]
	v_fma_mix_f32 v19, v59, v38, v19 op_sel:[1,0,0] op_sel_hi:[1,0,0]
	v_fma_mix_f32 v20, v60, v38, v20 op_sel_hi:[1,0,0]
	v_fma_mix_f32 v21, v60, v38, v21 op_sel:[1,0,0] op_sel_hi:[1,0,0]
	v_fma_mix_f32 v22, v61, v38, v22 op_sel_hi:[1,0,0]
	v_fma_mix_f32 v23, v61, v38, v23 op_sel:[1,0,0] op_sel_hi:[1,0,0]
	v_cvt_scalef32_pk_f16_fp8 v58, v50, 1.0
	v_cvt_scalef32_pk_f16_fp8 v59, v50, 1.0 op_sel:[1,0,0]
	v_cvt_scalef32_pk_f16_fp8 v60, v51, 1.0
	v_cvt_scalef32_pk_f16_fp8 v61, v51, 1.0 op_sel:[1,0,0]
	v_fma_mix_f32 v24, v58, v38, v24 op_sel_hi:[1,0,0]
	v_fma_mix_f32 v25, v58, v38, v25 op_sel:[1,0,0] op_sel_hi:[1,0,0]
	v_fma_mix_f32 v26, v59, v38, v26 op_sel_hi:[1,0,0]
	v_fma_mix_f32 v27, v59, v38, v27 op_sel:[1,0,0] op_sel_hi:[1,0,0]
	v_fma_mix_f32 v28, v60, v38, v28 op_sel_hi:[1,0,0]
	v_fma_mix_f32 v29, v60, v38, v29 op_sel:[1,0,0] op_sel_hi:[1,0,0]
	v_fma_mix_f32 v30, v61, v38, v30 op_sel_hi:[1,0,0]
	v_fma_mix_f32 v31, v61, v38, v31 op_sel:[1,0,0] op_sel_hi:[1,0,0]
	s_waitcnt vmcnt(0)
	v_cvt_scalef32_pk_f16_fp8 v58, v52, 1.0
	v_cvt_scalef32_pk_f16_fp8 v59, v52, 1.0 op_sel:[1,0,0]
	v_cvt_scalef32_pk_f16_fp8 v60, v53, 1.0
	v_cvt_scalef32_pk_f16_fp8 v61, v53, 1.0 op_sel:[1,0,0]
	v_fma_mix_f32 v16, v58, v39, v16 op_sel_hi:[1,0,0]
	v_fma_mix_f32 v17, v58, v39, v17 op_sel:[1,0,0] op_sel_hi:[1,0,0]
	v_fma_mix_f32 v18, v59, v39, v18 op_sel_hi:[1,0,0]
	v_fma_mix_f32 v19, v59, v39, v19 op_sel:[1,0,0] op_sel_hi:[1,0,0]
	v_fma_mix_f32 v20, v60, v39, v20 op_sel_hi:[1,0,0]
	v_fma_mix_f32 v21, v60, v39, v21 op_sel:[1,0,0] op_sel_hi:[1,0,0]
	v_fma_mix_f32 v22, v61, v39, v22 op_sel_hi:[1,0,0]
	v_fma_mix_f32 v23, v61, v39, v23 op_sel:[1,0,0] op_sel_hi:[1,0,0]
	v_cvt_scalef32_pk_f16_fp8 v58, v54, 1.0
	v_cvt_scalef32_pk_f16_fp8 v59, v54, 1.0 op_sel:[1,0,0]
	v_cvt_scalef32_pk_f16_fp8 v60, v55, 1.0
	v_cvt_scalef32_pk_f16_fp8 v61, v55, 1.0 op_sel:[1,0,0]
	v_fma_mix_f32 v24, v58, v39, v24 op_sel_hi:[1,0,0]
	v_fma_mix_f32 v25, v58, v39, v25 op_sel:[1,0,0] op_sel_hi:[1,0,0]
	v_fma_mix_f32 v26, v59, v39, v26 op_sel_hi:[1,0,0]
	v_fma_mix_f32 v27, v59, v39, v27 op_sel:[1,0,0] op_sel_hi:[1,0,0]
	v_fma_mix_f32 v28, v60, v39, v28 op_sel_hi:[1,0,0]
	v_fma_mix_f32 v29, v60, v39, v29 op_sel:[1,0,0] op_sel_hi:[1,0,0]
	v_fma_mix_f32 v30, v61, v39, v30 op_sel_hi:[1,0,0]
	v_fma_mix_f32 v31, v61, v39, v31 op_sel:[1,0,0] op_sel_hi:[1,0,0]
	s_sub_i32 s29, s29, 4
	s_branch .Lagg_B
.Lagg_A_half:
	s_waitcnt lgkmcnt(0)
	v_or_b32_e32 v32, v32, v1
	v_or_b32_e32 v33, v33, v1
	global_load_ushort v36, v32, s[6:7]
	global_load_ushort v37, v33, s[6:7]
	v_lshlrev_b32_e32 v32, 3, v32
	v_lshlrev_b32_e32 v33, 3, v33
	global_load_dwordx4 v[40:43], v32, s[4:5]
	global_load_dwordx4 v[44:47], v33, s[4:5]
	ds_swizzle_b32 v32, v5 offset:swizzle(BITMASK_PERM, "pp100")
	ds_swizzle_b32 v33, v5 offset:swizzle(BITMASK_PERM, "pp101")
	ds_swizzle_b32 v34, v5 offset:swizzle(BITMASK_PERM, "pp110")
	ds_swizzle_b32 v35, v5 offset:swizzle(BITMASK_PERM, "pp111")
	s_waitcnt vmcnt(2)
	v_fma_mix_f32 v36, v36, 1.0, v9 op_sel_hi:[1,0,0]
	v_fma_mix_f32 v37, v37, 1.0, v9 op_sel_hi:[1,0,0]
	v_mul_f32_e32 v58, 0x3e4ccccd, v36
	v_mul_f32_e32 v59, 0x3e4ccccd, v37
	v_max_f32_e32 v36, v36, v58
	v_max_f32_e32 v37, v37, v59
	v_max3_f32 v13, v12, v36, v37
	v_sub_f32_e32 v57, v12, v13
	v_sub_f32_e32 v36, v36, v13
	v_sub_f32_e32 v37, v37, v13
	v_exp_f32_e32 v57, v57
	v_exp_f32_e32 v36, v36
	v_exp_f32_e32 v37, v37
	v_fma_f32 v14, v14, v57, v36
	v_mul_f32_e32 v16, v16, v57
	v_mul_f32_e32 v17, v17, v57
	v_mul_f32_e32 v18, v18, v57
	v_mul_f32_e32 v19, v19, v57
	v_mul_f32_e32 v20, v20, v57
	v_mul_f32_e32 v21, v21, v57
	v_mul_f32_e32 v22, v22, v57
	v_mul_f32_e32 v23, v23, v57
	v_mul_f32_e32 v24, v24, v57
	v_mul_f32_e32 v25, v25, v57
	v_mul_f32_e32 v26, v26, v57
	v_mul_f32_e32 v27, v27, v57
	v_mul_f32_e32 v28, v28, v57
	v_mul_f32_e32 v29, v29, v57
	v_mul_f32_e32 v30, v30, v57
	v_mul_f32_e32 v31, v31, v57
	v_add_f32_e32 v14, v14, v37
	s_waitcnt vmcnt(1)
	v_cvt_scalef32_pk_f16_fp8 v58, v40, 1.0
	v_cvt_scalef32_pk_f16_fp8 v59, v40, 1.0 op_sel:[1,0,0]
	v_cvt_scalef32_pk_f16_fp8 v60, v41, 1.0
	v_cvt_scalef32_pk_f16_fp8 v61, v41, 1.0 op_sel:[1,0,0]
	v_fma_mix_f32 v16, v58, v36, v16 op_sel_hi:[1,0,0]
	v_fma_mix_f32 v17, v58, v36, v17 op_sel:[1,0,0] op_sel_hi:[1,0,0]
	v_fma_mix_f32 v18, v59, v36, v18 op_sel_hi:[1,0,0]
	v_fma_mix_f32 v19, v59, v36, v19 op_sel:[1,0,0] op_sel_hi:[1,0,0]
	v_fma_mix_f32 v20, v60, v36, v20 op_sel_hi:[1,0,0]
	v_fma_mix_f32 v21, v60, v36, v21 op_sel:[1,0,0] op_sel_hi:[1,0,0]
	v_fma_mix_f32 v22, v61, v36, v22 op_sel_hi:[1,0,0]
	v_fma_mix_f32 v23, v61, v36, v23 op_sel:[1,0,0] op_sel_hi:[1,0,0]
	v_cvt_scalef32_pk_f16_fp8 v58, v42, 1.0
	v_cvt_scalef32_pk_f16_fp8 v59, v42, 1.0 op_sel:[1,0,0]
	v_cvt_scalef32_pk_f16_fp8 v60, v43, 1.0
	v_cvt_scalef32_pk_f16_fp8 v61, v43, 1.0 op_sel:[1,0,0]
	v_fma_mix_f32 v24, v58, v36, v24 op_sel_hi:[1,0,0]
	v_fma_mix_f32 v25, v58, v36, v25 op_sel:[1,0,0] op_sel_hi:[1,0,0]
	v_fma_mix_f32 v26, v59, v36, v26 op_sel_hi:[1,0,0]
	v_fma_mix_f32 v27, v59, v36, v27 op_sel:[1,0,0] op_sel_hi:[1,0,0]
	v_fma_mix_f32 v28, v60, v36, v28 op_sel_hi:[1,0,0]
	v_fma_mix_f32 v29, v60, v36, v29 op_sel:[1,0,0] op_sel_hi:[1,0,0]
	v_fma_mix_f32 v30, v61, v36, v30 op_sel_hi:[1,0,0]
	v_fma_mix_f32 v31, v61, v36, v31 op_sel:[1,0,0] op_sel_hi:[1,0,0]
	s_waitcnt vmcnt(0)
	v_cvt_scalef32_pk_f16_fp8 v58, v44, 1.0
	v_cvt_scalef32_pk_f16_fp8 v59, v44, 1.0 op_sel:[1,0,0]
	v_cvt_scalef32_pk_f16_fp8 v60, v45, 1.0
	v_cvt_scalef32_pk_f16_fp8 v61, v45, 1.0 op_sel:[1,0,0]
	v_fma_mix_f32 v16, v58, v37, v16 op_sel_hi:[1,0,0]
	v_fma_mix_f32 v17, v58, v37, v17 op_sel:[1,0,0] op_sel_hi:[1,0,0]
	v_fma_mix_f32 v18, v59, v37, v18 op_sel_hi:[1,0,0]
	v_fma_mix_f32 v19, v59, v37, v19 op_sel:[1,0,0] op_sel_hi:[1,0,0]
	v_fma_mix_f32 v20, v60, v37, v20 op_sel_hi:[1,0,0]
	v_fma_mix_f32 v21, v60, v37, v21 op_sel:[1,0,0] op_sel_hi:[1,0,0]
	v_fma_mix_f32 v22, v61, v37, v22 op_sel_hi:[1,0,0]
	v_fma_mix_f32 v23, v61, v37, v23 op_sel:[1,0,0] op_sel_hi:[1,0,0]
	v_cvt_scalef32_pk_f16_fp8 v58, v46, 1.0
	v_cvt_scalef32_pk_f16_fp8 v59, v46, 1.0 op_sel:[1,0,0]
	v_cvt_scalef32_pk_f16_fp8 v60, v47, 1.0
	v_cvt_scalef32_pk_f16_fp8 v61, v47, 1.0 op_sel:[1,0,0]
	v_fma_mix_f32 v24, v58, v37, v24 op_sel_hi:[1,0,0]
	v_fma_mix_f32 v25, v58, v37, v25 op_sel:[1,0,0] op_sel_hi:[1,0,0]
	v_fma_mix_f32 v26, v59, v37, v26 op_sel_hi:[1,0,0]
	v_fma_mix_f32 v27, v59, v37, v27 op_sel:[1,0,0] op_sel_hi:[1,0,0]
	v_fma_mix_f32 v28, v60, v37, v28 op_sel_hi:[1,0,0]
	v_fma_mix_f32 v29, v60, v37, v29 op_sel:[1,0,0] op_sel_hi:[1,0,0]
	v_fma_mix_f32 v30, v61, v37, v30 op_sel_hi:[1,0,0]
	v_fma_mix_f32 v31, v61, v37, v31 op_sel:[1,0,0] op_sel_hi:[1,0,0]
	s_branch .Lagg_epi
.Lagg_B_half:
	s_waitcnt lgkmcnt(0)
	v_or_b32_e32 v32, v32, v1
	v_or_b32_e32 v33, v33, v1
	global_load_ushort v36, v32, s[6:7]
	global_load_ushort v37, v33, s[6:7]
	v_lshlrev_b32_e32 v32, 3, v32
	v_lshlrev_b32_e32 v33, 3, v33
	global_load_dwordx4 v[40:43], v32, s[4:5]
	global_load_dwordx4 v[44:47], v33, s[4:5]
	ds_swizzle_b32 v32, v5 offset:swizzle(BITMASK_PERM, "pp100")
	ds_swizzle_b32 v33, v5 offset:swizzle(BITMASK_PERM, "pp101")
	ds_swizzle_b32 v34, v5 offset:swizzle(BITMASK_PERM, "pp110")
	ds_swizzle_b32 v35, v5 offset:swizzle(BITMASK_PERM, "pp111")
	s_waitcnt vmcnt(2)
	v_fma_mix_f32 v36, v36, 1.0, v9 op_sel_hi:[1,0,0]
	v_fma_mix_f32 v37, v37, 1.0, v9 op_sel_hi:[1,0,0]
	v_mul_f32_e32 v58, 0x3e4ccccd, v36
	v_mul_f32_e32 v59, 0x3e4ccccd, v37
	v_max_f32_e32 v36, v36, v58
	v_max_f32_e32 v37, v37, v59
	v_max3_f32 v12, v13, v36, v37
	v_sub_f32_e32 v57, v13, v12
	v_sub_f32_e32 v36, v36, v12
	v_sub_f32_e32 v37, v37, v12
	v_exp_f32_e32 v57, v57
	v_exp_f32_e32 v36, v36
	v_exp_f32_e32 v37, v37
	v_fma_f32 v14, v14, v57, v36
	v_mul_f32_e32 v16, v16, v57
	v_mul_f32_e32 v17, v17, v57
	v_mul_f32_e32 v18, v18, v57
	v_mul_f32_e32 v19, v19, v57
	v_mul_f32_e32 v20, v20, v57
	v_mul_f32_e32 v21, v21, v57
	v_mul_f32_e32 v22, v22, v57
	v_mul_f32_e32 v23, v23, v57
	v_mul_f32_e32 v24, v24, v57
	v_mul_f32_e32 v25, v25, v57
	v_mul_f32_e32 v26, v26, v57
	v_mul_f32_e32 v27, v27, v57
	v_mul_f32_e32 v28, v28, v57
	v_mul_f32_e32 v29, v29, v57
	v_mul_f32_e32 v30, v30, v57
	v_mul_f32_e32 v31, v31, v57
	v_add_f32_e32 v14, v14, v37
	s_waitcnt vmcnt(1)
	v_cvt_scalef32_pk_f16_fp8 v58, v40, 1.0
	v_cvt_scalef32_pk_f16_fp8 v59, v40, 1.0 op_sel:[1,0,0]
	v_cvt_scalef32_pk_f16_fp8 v60, v41, 1.0
	v_cvt_scalef32_pk_f16_fp8 v61, v41, 1.0 op_sel:[1,0,0]
	v_fma_mix_f32 v16, v58, v36, v16 op_sel_hi:[1,0,0]
	v_fma_mix_f32 v17, v58, v36, v17 op_sel:[1,0,0] op_sel_hi:[1,0,0]
	v_fma_mix_f32 v18, v59, v36, v18 op_sel_hi:[1,0,0]
	v_fma_mix_f32 v19, v59, v36, v19 op_sel:[1,0,0] op_sel_hi:[1,0,0]
	v_fma_mix_f32 v20, v60, v36, v20 op_sel_hi:[1,0,0]
	v_fma_mix_f32 v21, v60, v36, v21 op_sel:[1,0,0] op_sel_hi:[1,0,0]
	v_fma_mix_f32 v22, v61, v36, v22 op_sel_hi:[1,0,0]
	v_fma_mix_f32 v23, v61, v36, v23 op_sel:[1,0,0] op_sel_hi:[1,0,0]
	v_cvt_scalef32_pk_f16_fp8 v58, v42, 1.0
	v_cvt_scalef32_pk_f16_fp8 v59, v42, 1.0 op_sel:[1,0,0]
	v_cvt_scalef32_pk_f16_fp8 v60, v43, 1.0
	v_cvt_scalef32_pk_f16_fp8 v61, v43, 1.0 op_sel:[1,0,0]
	v_fma_mix_f32 v24, v58, v36, v24 op_sel_hi:[1,0,0]
	v_fma_mix_f32 v25, v58, v36, v25 op_sel:[1,0,0] op_sel_hi:[1,0,0]
	v_fma_mix_f32 v26, v59, v36, v26 op_sel_hi:[1,0,0]
	v_fma_mix_f32 v27, v59, v36, v27 op_sel:[1,0,0] op_sel_hi:[1,0,0]
	v_fma_mix_f32 v28, v60, v36, v28 op_sel_hi:[1,0,0]
	v_fma_mix_f32 v29, v60, v36, v29 op_sel:[1,0,0] op_sel_hi:[1,0,0]
	v_fma_mix_f32 v30, v61, v36, v30 op_sel_hi:[1,0,0]
	v_fma_mix_f32 v31, v61, v36, v31 op_sel:[1,0,0] op_sel_hi:[1,0,0]
	s_waitcnt vmcnt(0)
	v_cvt_scalef32_pk_f16_fp8 v58, v44, 1.0
	v_cvt_scalef32_pk_f16_fp8 v59, v44, 1.0 op_sel:[1,0,0]
	v_cvt_scalef32_pk_f16_fp8 v60, v45, 1.0
	v_cvt_scalef32_pk_f16_fp8 v61, v45, 1.0 op_sel:[1,0,0]
	v_fma_mix_f32 v16, v58, v37, v16 op_sel_hi:[1,0,0]
	v_fma_mix_f32 v17, v58, v37, v17 op_sel:[1,0,0] op_sel_hi:[1,0,0]
	v_fma_mix_f32 v18, v59, v37, v18 op_sel_hi:[1,0,0]
	v_fma_mix_f32 v19, v59, v37, v19 op_sel:[1,0,0] op_sel_hi:[1,0,0]
	v_fma_mix_f32 v20, v60, v37, v20 op_sel_hi:[1,0,0]
	v_fma_mix_f32 v21, v60, v37, v21 op_sel:[1,0,0] op_sel_hi:[1,0,0]
	v_fma_mix_f32 v22, v61, v37, v22 op_sel_hi:[1,0,0]
	v_fma_mix_f32 v23, v61, v37, v23 op_sel:[1,0,0] op_sel_hi:[1,0,0]
	v_cvt_scalef32_pk_f16_fp8 v58, v46, 1.0
	v_cvt_scalef32_pk_f16_fp8 v59, v46, 1.0 op_sel:[1,0,0]
	v_cvt_scalef32_pk_f16_fp8 v60, v47, 1.0
	v_cvt_scalef32_pk_f16_fp8 v61, v47, 1.0 op_sel:[1,0,0]
	v_fma_mix_f32 v24, v58, v37, v24 op_sel_hi:[1,0,0]
	v_fma_mix_f32 v25, v58, v37, v25 op_sel:[1,0,0] op_sel_hi:[1,0,0]
	v_fma_mix_f32 v26, v59, v37, v26 op_sel_hi:[1,0,0]
	v_fma_mix_f32 v27, v59, v37, v27 op_sel:[1,0,0] op_sel_hi:[1,0,0]
	v_fma_mix_f32 v28, v60, v37, v28 op_sel_hi:[1,0,0]
	v_fma_mix_f32 v29, v60, v37, v29 op_sel:[1,0,0] op_sel_hi:[1,0,0]
	v_fma_mix_f32 v30, v61, v37, v30 op_sel_hi:[1,0,0]
	v_fma_mix_f32 v31, v61, v37, v31 op_sel:[1,0,0] op_sel_hi:[1,0,0]
